# attention main loop: one static priority raise for waves 4-7 for the duration of a unit (no per-segment toggling)
# baseline (speedup 1.0000x reference)
; __global__ void __launch_bounds__(NWAVES * 64, 2) mega_fwd(Args args) {
;     ...
;             for (int pa_ = 0; pa_ <= PROBE_ATT2; ++pa_) for (;;) {
;                 if (F.tid == 0) QS[0] = (int)__hip_atomic_fetch_add(F.ctl + CW_Q + 64 * F.l + 4 * pa_, 1u, __ATOMIC_RELAXED, __HIP_MEMORY_SCOPE_AGENT);
;                 __syncthreads();
;                 const int idx = __builtin_amdgcn_readfirstlane(QS[0]);
.LBB0_2753:
	s_setprio 0
	s_and_saveexec_b64 s[0:1], s[2:3]
	s_cbranch_execz .LBB0_2757
	s_mov_b64 s[24:25], exec
	v_mbcnt_lo_u32_b32 v0, s24, 0
	v_mbcnt_hi_u32_b32 v1, s25, v0
	v_cmp_eq_u32_e32 vcc, 0, v1
	s_and_saveexec_b64 s[4:5], vcc
	s_cbranch_execz .LBB0_2756
	s_bcnt1_i32_b64 s24, s[24:25]
	v_mov_b32_e32 v0, s24
	s_waitcnt vmcnt(0)
	v_mov_b32_e32 v2, v200

; template<int THRL> __device__ __forceinline__ void attn_unit(int b,int h,int qb,const bf16*Q,const bf16*__restrict__ K,const bf16*__restrict__ V,bf16*O,const float*__restrict__ F2g,const float*__restrict__ gain,float qkb,char*shm){
;   int tid_=threadIdx.x; asm volatile("":"+v"(tid_)); const int tid=tid_,lane=tid&63,r32=lane&31,hi=lane>>5; const int wid=__builtin_amdgcn_readfirstlane(tid>>6);
;   const long rowbase=(long)b*SEQ; const int q0=qb*QB;
;   const bf16*Qw=Q+(rowbase+q0+wid*QBLK)*DM+h*D;
;   const float*f2row=F2g+((long)b*NHEAD+h)*SEQ;
;   int t0;
;   { const int NTf=(q0+QB)/KVBLK; const float thr=f2row[q0]+qkb+40.0f; const int ta=lane,tb=lane+64;
;     const bool va=(ta<NTf-4)&&(f2row[64*ta+63]>thr), vb=(tb<NTf-4)&&(f2row[64*tb+63]>thr);
;     t0=(__builtin_popcountll(__ballot(va))+__builtin_popcountll(__ballot(vb)))&~1; t0=__builtin_amdgcn_readfirstlane(t0); }
; __global__ void __launch_bounds__(NWAVES * 64, 2) mega_fwd(Args args) {
;     ...
;                 if (F.tid == 0) QS[0] = (int)__hip_atomic_fetch_add(F.ctl + CW_Q + 64 * F.l + 4 * pa_, 1u, __ATOMIC_RELAXED, __HIP_MEMORY_SCOPE_AGENT);
;                 __syncthreads();
;                 const int idx = __builtin_amdgcn_readfirstlane(QS[0]);
;                 __syncthreads();
;                 if (idx >= ((QMODE >= 2) ? 512 : 512 + 2560)) break;
;                 if (idx < 512) { const attn_body::AttnUnit u{(idx & 3) * 4 + 3 - ((idx >> 2) & 3), 31 - (idx >> 4)};
;                     attn_body::attn_unit<8>(u.bh / 4, u.bh % 4, u.qb, AT.Q, AT.K, AT.V, AT.O, AT.F2, AT.gain, 2.0f * sqrtf(__uint_as_float(AT.qkn[2 * u.bh]) * __uint_as_float(AT.qkn[2 * u.bh + 1])), (char*)lds); }
.LBB0_2757:
	s_or_b64 exec, exec, s[0:1]
	v_mov_b32_e32 v0, s17
	s_waitcnt vmcnt(0) lgkmcnt(0)
	s_barrier
	ds_read_b32 v0, v0
	s_mov_b64 s[0:1], -1
	s_waitcnt lgkmcnt(0)
	s_barrier
	v_readfirstlane_b32 s4, v0
	s_cmpk_gt_i32 s4, 0x1ff
	s_cbranch_scc1 .LBB0_2752
	v_readfirstlane_b32 s62, v228
	s_cmp_gt_u32 s62, 255
	s_cbranch_scc0 .Lmy_att_noprio
	s_setprio 1
.Lmy_att_noprio:
	s_lshl_b32 s0, s4, 2
	s_and_b32 s0, s0, 12
	s_or_b32 s0, s0, 3
	s_bfe_u32 s1, s4, 0x20002
	s_sub_i32 s0, s0, s1
	s_lshr_b32 s55, s0, 2
	s_and_b32 s28, s0, 3
	s_lshl_b32 s0, s0, 3
	v_mov_b32_e32 v0, s0
	global_load_dwordx2 v[0:1], v0, s[6:7]
	s_lshl_b32 s78, s4, 4
	s_and_b32 s78, s78, 0xffffff00
	s_sub_i32 s78, 0x1f00, s78
	s_lshl_b32 s74, s55, 17
	s_add_u32 s74, s45, s74
	s_addc_u32 s75, s47, 0
	s_lshl_b32 s79, s28, 15
	s_add_u32 s74, s74, s79
	s_addc_u32 s75, s75, 0
	s_lshl_b32 s78, s78, 2
	s_add_u32 s76, s74, s78
	s_addc_u32 s77, s75, 0
	v_and_b32_e32 v9, 63, v228
	v_lshlrev_b32_e32 v9, 8, v9
	global_load_dword v6, v3, s[76:77]
	global_load_dword v7, v9, s[74:75] offset:252
	v_or_b32_e32 v9, 0x4000, v9
	global_load_dword v8, v9, s[74:75] offset:252
	s_mov_b32 s0, 0xf800000
	v_mov_b32_e32 v50, v228
	s_mov_b64 s[24:25], 0
	v_and_b32_e32 v131, 63, v50
	v_readfirstlane_b32 s35, v50
	s_waitcnt vmcnt(0)
	v_mul_f32_e32 v0, v0, v1
	v_cmp_gt_f32_e32 vcc, s0, v0
	v_mul_f32_e32 v1, 0x4f800000, v0
	s_nop 0
	v_cndmask_b32_e32 v0, v0, v1, vcc
	v_sqrt_f32_e32 v1, v0
	s_nop 0
	v_add_u32_e32 v2, -1, v1
	v_fma_f32 v4, -v2, v1, v0
	v_cmp_ge_f32_e64 s[0:1], 0, v4
	v_add_u32_e32 v4, 1, v1
	s_nop 0
	v_cndmask_b32_e64 v2, v1, v2, s[0:1]
	v_fma_f32 v1, -v4, v1, v0
	v_cmp_lt_f32_e64 s[0:1], 0, v1
	s_nop 1
	v_cndmask_b32_e64 v1, v2, v4, s[0:1]
	s_lshl_b32 s0, s4, 4
	s_and_b32 s29, s0, 0xffffff00
	s_sub_i32 s52, 0x1f00, s29
	s_lshl_b32 s0, s55, 17
	s_add_u32 s0, s45, s0
	s_addc_u32 s1, s47, 0
	s_lshl_b32 s4, s28, 15
	s_add_u32 s0, s0, s4
	s_addc_u32 s1, s1, 0
	s_sub_i32 s4, 0x2000, s29
	v_mul_f32_e32 v2, 0x37800000, v1
	s_lshr_b32 s30, s4, 6
	s_lshl_b64 s[4:5], s[52:53], 2
	v_cndmask_b32_e32 v1, v1, v2, vcc
	v_mov_b32_e32 v2, 0x260
	s_add_u32 s4, s0, s4
	v_cmp_class_f32_e32 vcc, v0, v2
	s_addc_u32 s5, s1, s5
	s_add_i32 s31, s30, -4
	v_cndmask_b32_e32 v0, v1, v0, vcc
	v_mov_b32_e32 v1, v6
	v_cmp_gt_u32_e32 vcc, s31, v131
	s_mov_b64 s[4:5], 0
	s_waitcnt vmcnt(0)
	v_fmac_f32_e32 v1, 2.0, v0
	v_add_f32_e32 v1, 0x42200000, v1
	s_and_saveexec_b64 s[26:27], vcc
	s_cbranch_execz .LBB0_2760
	v_lshlrev_b32_e32 v0, 8, v131
	v_mov_b32_e32 v0, v7
	s_waitcnt vmcnt(0)
	v_cmp_gt_f32_e32 vcc, v0, v1
	s_and_b64 s[24:25], vcc, exec
